# plus mlstm_a K/V prefetch at unit top and mlstm_c q prefetch
# speedup vs baseline: 1.0164x; 1.0029x over previous
.LBB0_476:
	s_or_b64 exec, exec, s[52:53]
	s_ashr_i32 s51, s50, 31
	s_lshl_b64 s[50:51], s[50:51], 8
	v_mov_b32_e32 v3, s51
	v_or_b32_e32 v2, s50, v14
	s_lshl_b32 s26, s3, 1
	v_lshl_add_u64 v[6:7], v[2:3], 0, s[28:29]
	v_lshl_add_u64 v[2:3], v[2:3], 0, s[30:31]
	v_lshl_add_u64 v[4:5], v[22:23], 0, s[26:27]
	v_lshlrev_b64 v[6:7], 14, v[6:7]
	v_lshlrev_b64 v[2:3], 14, v[2:3]
	v_lshl_add_u64 v[100:101], v[4:5], 0, v[6:7]
	v_lshl_add_u64 v[104:105], v[4:5], 0, v[2:3]
	s_waitcnt vmcnt(4)
	v_mov_b32_e32 v10, v156
	v_mov_b32_e32 v11, v157
	v_mov_b32_e32 v12, v158
	v_mov_b32_e32 v13, v159
	v_mov_b32_e32 v60, v160
	v_mov_b32_e32 v61, v161
	v_mov_b32_e32 v62, v162
	v_mov_b32_e32 v63, v163
	v_mov_b32_e32 v2, v164
	v_mov_b32_e32 v3, v165
	v_mov_b32_e32 v4, v166
	v_mov_b32_e32 v5, v167
	v_mov_b32_e32 v6, v168
	v_mov_b32_e32 v7, v169
	v_mov_b32_e32 v8, v170
	v_mov_b32_e32 v9, v171
	ds_read_b128 v[56:59], v38
	ds_read_b128 v[64:67], v38 offset:64
	ds_read_b128 v[72:75], v38 offset:4352
	ds_read_b128 v[76:79], v38 offset:4416
	ds_read_b128 v[84:87], v38 offset:8704
	ds_read_b128 v[88:91], v38 offset:8768
	ds_read_b128 v[96:99], v38 offset:128
	v_lshlrev_b64 v[34:35], 8, v[34:35]
	v_or_b32_e32 v34, v34, v14
	s_add_u32 s48, s48, s84
	s_addc_u32 s49, s49, s85
	s_add_u32 s34, s34, s36
	s_addc_u32 s35, s35, s37
	s_add_i32 s33, s33, s41
	v_lshl_add_u64 v[26:27], v[26:27], 0, s[38:39]
	s_cmpk_lt_i32 s48, 0x600
	v_lshl_add_u64 v[28:29], v[28:29], 0, s[38:39]
	s_waitcnt lgkmcnt(6)
	v_mfma_f32_16x16x32_bf16 v[68:71], v[56:59], v[10:13], 0
	s_nop 0
	v_mfma_f32_16x16x32_bf16 v[56:59], v[56:59], v[2:5], 0
	s_waitcnt lgkmcnt(4)
	v_mfma_f32_16x16x32_bf16 v[80:83], v[72:75], v[10:13], 0
	v_mfma_f32_16x16x32_bf16 v[72:75], v[72:75], v[2:5], 0
	v_mfma_f32_16x16x32_bf16 v[68:71], v[64:67], v[60:63], v[68:71]
	s_nop 0
	v_mfma_f32_16x16x32_bf16 v[56:59], v[64:67], v[6:9], v[56:59]
	s_waitcnt lgkmcnt(3)
	v_mfma_f32_16x16x32_bf16 v[64:67], v[76:79], v[60:63], v[80:83]
	s_nop 2
	s_waitcnt vmcnt(0)
	v_mov_b32_e32 v80, v172
	v_mov_b32_e32 v81, v173
	v_mov_b32_e32 v82, v174
	v_mov_b32_e32 v83, v175
	v_mfma_f32_16x16x32_bf16 v[72:75], v[76:79], v[6:9], v[72:75]
	v_mov_b32_e32 v76, v176
	v_mov_b32_e32 v77, v177
	v_mov_b32_e32 v78, v178
	v_mov_b32_e32 v79, v179
	s_nop 0
	v_mov_b32_e32 v104, v180
	v_mov_b32_e32 v105, v181
	v_mov_b32_e32 v106, v182
	v_mov_b32_e32 v107, v183
	s_waitcnt lgkmcnt(2)
	v_mfma_f32_16x16x32_bf16 v[92:95], v[84:87], v[10:13], 0
	v_mfma_f32_16x16x32_bf16 v[84:87], v[84:87], v[2:5], 0
	s_waitcnt lgkmcnt(1)
	v_mfma_f32_16x16x32_bf16 v[92:95], v[88:91], v[60:63], v[92:95]
	v_mfma_f32_16x16x32_bf16 v[84:87], v[88:91], v[6:9], v[84:87]
	v_mov_b32_e32 v88, v184
	v_mov_b32_e32 v89, v185
	v_mov_b32_e32 v90, v186
	v_mov_b32_e32 v91, v187
	ds_read_b128 v[100:103], v38 offset:192
	s_waitcnt lgkmcnt(1)
	v_mfma_f32_16x16x32_bf16 v[68:71], v[96:99], v[80:83], v[68:71]
	s_nop 0
	v_mfma_f32_16x16x32_bf16 v[56:59], v[96:99], v[76:79], v[56:59]
	ds_read_b128 v[96:99], v38 offset:4480
	ds_read_b128 v[108:111], v38 offset:4544
	s_waitcnt lgkmcnt(1)
	v_mfma_f32_16x16x32_bf16 v[64:67], v[96:99], v[80:83], v[64:67]
	v_mfma_f32_16x16x32_bf16 v[72:75], v[96:99], v[76:79], v[72:75]
	ds_read_b128 v[96:99], v38 offset:8832
	ds_read_b128 v[112:115], v38 offset:8896
	ds_read_b128 v[116:119], v38 offset:13248
	ds_read_b128 v[120:123], v38 offset:17536
	ds_read_b128 v[124:127], v38 offset:17600
	s_waitcnt lgkmcnt(4)
	v_mfma_f32_16x16x32_bf16 v[92:95], v[96:99], v[80:83], v[92:95]
	ds_read_b128 v[128:131], v38 offset:21888
	ds_read_b128 v[132:135], v38 offset:21952
	v_mfma_f32_16x16x32_bf16 v[84:87], v[96:99], v[76:79], v[84:87]
	ds_read_b128 v[96:99], v38 offset:13056
	s_nop 0
	v_mfma_f32_16x16x32_bf16 v[68:71], v[100:103], v[88:91], v[68:71]
	v_mfma_f32_16x16x32_bf16 v[56:59], v[100:103], v[104:107], v[56:59]
	ds_read_b128 v[100:103], v38 offset:13120
	s_nop 5
	v_cvt_pk_bf16_f32 v136, v68, v69
	v_cvt_pk_bf16_f32 v137, v70, v71
	s_waitcnt lgkmcnt(7)
	v_mfma_f32_16x16x32_bf16 v[92:95], v[112:115], v[88:91], v[92:95]
	v_mfma_f32_16x16x32_bf16 v[84:87], v[112:115], v[104:107], v[84:87]
	ds_read_b128 v[112:115], v38 offset:13184
	v_mfma_f32_16x16x32_bf16 v[64:67], v[108:111], v[88:91], v[64:67]
	v_mfma_f32_16x16x32_bf16 v[72:75], v[108:111], v[104:107], v[72:75]
	s_nop 4
	v_cvt_pk_bf16_f32 v84, v84, v85
	v_cvt_pk_bf16_f32 v85, v86, v87
	v_cvt_pk_bf16_f32 v64, v64, v65
	s_waitcnt lgkmcnt(2)
	v_mfma_f32_16x16x32_bf16 v[108:111], v[96:99], v[10:13], 0
	v_cvt_pk_bf16_f32 v65, v66, v67
	v_cvt_pk_bf16_f32 v72, v72, v73
	v_cvt_pk_bf16_f32 v73, v74, v75
	v_mfma_f32_16x16x32_bf16 v[96:99], v[96:99], v[2:5], 0
	s_waitcnt lgkmcnt(1)
	v_mfma_f32_16x16x32_bf16 v[108:111], v[100:103], v[60:63], v[108:111]
	v_mfma_f32_16x16x32_bf16 v[96:99], v[100:103], v[6:9], v[96:99]
	ds_read_b128 v[100:103], v38 offset:17408
	s_waitcnt lgkmcnt(1)
	v_mfma_f32_16x16x32_bf16 v[108:111], v[112:115], v[80:83], v[108:111]
	v_mfma_f32_16x16x32_bf16 v[96:99], v[112:115], v[76:79], v[96:99]
	ds_read_b128 v[112:115], v38 offset:17472
	v_mfma_f32_16x16x32_bf16 v[108:111], v[116:119], v[88:91], v[108:111]
	v_mfma_f32_16x16x32_bf16 v[96:99], v[116:119], v[104:107], v[96:99]
	s_waitcnt lgkmcnt(1)
	v_mfma_f32_16x16x32_bf16 v[116:119], v[100:103], v[10:13], 0
	v_mfma_f32_16x16x32_bf16 v[100:103], v[100:103], v[2:5], 0
	s_waitcnt lgkmcnt(0)
	v_mfma_f32_16x16x32_bf16 v[116:119], v[112:115], v[60:63], v[116:119]
	v_mfma_f32_16x16x32_bf16 v[100:103], v[112:115], v[6:9], v[100:103]
	ds_read_b128 v[112:115], v38 offset:21760
	v_mfma_f32_16x16x32_bf16 v[116:119], v[120:123], v[80:83], v[116:119]
	v_mfma_f32_16x16x32_bf16 v[100:103], v[120:123], v[76:79], v[100:103]
	ds_read_b128 v[120:123], v38 offset:21824
	v_mfma_f32_16x16x32_bf16 v[116:119], v[124:127], v[88:91], v[116:119]
	v_mfma_f32_16x16x32_bf16 v[100:103], v[124:127], v[104:107], v[100:103]
	s_waitcnt lgkmcnt(1)
	v_mfma_f32_16x16x32_bf16 v[124:127], v[112:115], v[10:13], 0
	v_mfma_f32_16x16x32_bf16 v[68:71], v[112:115], v[2:5], 0
	v_lshl_add_u64 v[112:113], v[34:35], 0, s[28:29]
	v_lshlrev_b64 v[112:113], 8, v[112:113]
	v_lshl_add_u64 v[138:139], v[24:25], 0, v[112:113]
	ds_read_b128 v[112:115], v38 offset:26112
	global_store_dwordx2 v[138:139], v[136:137], off
	v_cvt_pk_bf16_f32 v136, v56, v57
	v_cvt_pk_bf16_f32 v137, v58, v59
	ds_read_b128 v[56:59], v38 offset:26176
	s_waitcnt lgkmcnt(2)
	v_mfma_f32_16x16x32_bf16 v[124:127], v[120:123], v[60:63], v[124:127]
	v_lshl_add_u64 v[34:35], v[34:35], 0, s[30:31]
	v_lshlrev_b64 v[34:35], 8, v[34:35]
	v_lshl_add_u64 v[34:35], v[24:25], 0, v[34:35]
	v_mfma_f32_16x16x32_bf16 v[68:71], v[120:123], v[6:9], v[68:71]
	global_store_dwordx2 v[34:35], v[72:73], off offset:32
	v_cvt_pk_bf16_f32 v72, v92, v93
	v_cvt_pk_bf16_f32 v73, v94, v95
	v_mfma_f32_16x16x32_bf16 v[124:127], v[128:131], v[80:83], v[124:127]
	global_store_dwordx2 v[138:139], v[72:73], off offset:64
	global_store_dwordx2 v[34:35], v[84:85], off offset:64
	v_cvt_pk_bf16_f32 v84, v108, v109
	v_mfma_f32_16x16x32_bf16 v[68:71], v[128:131], v[76:79], v[68:71]
	v_cvt_pk_bf16_f32 v85, v110, v111
	global_store_dwordx2 v[138:139], v[84:85], off offset:96
	ds_read_b128 v[84:87], v38 offset:30528
	s_waitcnt lgkmcnt(2)
	v_mfma_f32_16x16x32_bf16 v[128:131], v[112:115], v[10:13], 0
	ds_read_b128 v[120:123], v38 offset:26240
	v_cvt_pk_bf16_f32 v92, v96, v97
	v_cvt_pk_bf16_f32 v93, v98, v99
	v_mfma_f32_16x16x32_bf16 v[72:75], v[112:115], v[2:5], 0
	global_store_dwordx2 v[34:35], v[92:93], off offset:96
	ds_read_b128 v[92:95], v38 offset:30592
	v_cvt_pk_bf16_f32 v96, v116, v117
	s_waitcnt lgkmcnt(3)
	v_mfma_f32_16x16x32_bf16 v[128:131], v[56:59], v[60:63], v[128:131]
	v_cvt_pk_bf16_f32 v97, v118, v119
	global_store_dwordx2 v[138:139], v[96:97], off offset:128
	ds_read_b128 v[96:99], v38 offset:30656
	v_mfma_f32_16x16x32_bf16 v[56:59], v[56:59], v[6:9], v[72:75]
	global_store_dwordx2 v[138:139], v[64:65], off offset:32
	global_store_dwordx2 v[34:35], v[136:137], off
	s_nop 0
	ds_read_b128 v[72:75], v38 offset:30464
	s_waitcnt lgkmcnt(0)
	v_mfma_f32_16x16x32_bf16 v[10:13], v[72:75], v[10:13], 0
	v_mfma_f32_16x16x32_bf16 v[2:5], v[72:75], v[2:5], 0
	v_mfma_f32_16x16x32_bf16 v[124:127], v[132:135], v[88:91], v[124:127]
	v_mfma_f32_16x16x32_bf16 v[68:71], v[132:135], v[104:107], v[68:71]
	ds_read_b128 v[132:135], v38 offset:26304
	v_mfma_f32_16x16x32_bf16 v[10:13], v[84:87], v[60:63], v[10:13]
	v_cvt_pk_bf16_f32 v60, v100, v101
	v_cvt_pk_bf16_f32 v61, v102, v103
	global_store_dwordx2 v[34:35], v[60:61], off offset:128
	v_mfma_f32_16x16x32_bf16 v[2:5], v[84:87], v[6:9], v[2:5]
	s_nop 0
	v_cvt_pk_bf16_f32 v60, v124, v125
	v_cvt_pk_bf16_f32 v61, v126, v127
	global_store_dwordx2 v[138:139], v[60:61], off offset:160
	v_mfma_f32_16x16x32_bf16 v[56:59], v[120:123], v[76:79], v[56:59]
	v_cvt_pk_bf16_f32 v60, v68, v69
	v_cvt_pk_bf16_f32 v61, v70, v71
	global_store_dwordx2 v[34:35], v[60:61], off offset:160
	v_mfma_f32_16x16x32_bf16 v[64:67], v[120:123], v[80:83], v[128:131]
	v_mfma_f32_16x16x32_bf16 v[10:13], v[92:95], v[80:83], v[10:13]
	v_mfma_f32_16x16x32_bf16 v[2:5], v[92:95], v[76:79], v[2:5]
	s_waitcnt lgkmcnt(0)
	v_mfma_f32_16x16x32_bf16 v[56:59], v[132:135], v[104:107], v[56:59]
	v_mfma_f32_16x16x32_bf16 v[64:67], v[132:135], v[88:91], v[64:67]
	v_mfma_f32_16x16x32_bf16 v[10:13], v[96:99], v[88:91], v[10:13]
	s_nop 5
	v_cvt_pk_bf16_f32 v6, v56, v57
	v_cvt_pk_bf16_f32 v7, v58, v59
	v_cvt_pk_bf16_f32 v60, v64, v65
	v_mfma_f32_16x16x32_bf16 v[2:5], v[96:99], v[104:107], v[2:5]
	v_cvt_pk_bf16_f32 v61, v66, v67
	global_store_dwordx2 v[34:35], v[6:7], off offset:192
	v_cvt_pk_bf16_f32 v6, v10, v11
	v_cvt_pk_bf16_f32 v7, v12, v13
	global_store_dwordx2 v[138:139], v[60:61], off offset:192
	s_nop 2
	v_cvt_pk_bf16_f32 v2, v2, v3
	v_cvt_pk_bf16_f32 v3, v4, v5
	global_store_dwordx2 v[138:139], v[6:7], off offset:224
	global_store_dwordx2 v[34:35], v[2:3], off offset:224
	s_barrier
	s_cbranch_scc0 .LBB0_485
.LBB0_477:
	s_ashr_i32 s50, s48, 6
	s_mul_hi_i32 s3, s50, 0x2aaaaaab
	s_lshr_b32 s26, s3, 31
	s_add_i32 s54, s3, s26
	s_mul_i32 s3, s54, 6
	s_ashr_i32 s55, s54, 31
	s_sub_i32 s52, s50, s3
	s_lshl_b64 s[54:55], s[54:55], 13
	s_and_b32 s3, s33, 0x1f80
	s_and_b64 vcc, exec, s[18:19]
	s_or_b32 s54, s54, s3
	v_lshl_add_u64 v[194:195], s[54:55], 0, v[20:21]
	v_mov_b64_e32 v[196:197], s[24:25]
	v_mad_u64_u32 v[196:197], s[98:99], v194, s65, v[196:197]
	v_mov_b32_e32 v194, v197
	v_mad_u64_u32 v[194:195], s[98:99], v195, s65, v[194:195]
	s_lshl_b32 s100, s52, 7
	v_mov_b32_e32 v197, v194
	s_ashr_i32 s101, s100, 31
	v_lshl_add_u64 v[194:195], s[100:101], 1, v[196:197]
	v_lshl_add_u64 v[188:189], v[194:195], 0, v[18:19]
	global_load_dwordx4 v[140:143], v[188:189], off
	global_load_dwordx4 v[144:147], v[188:189], off offset:16
	global_load_dwordx4 v[148:151], v[188:189], off offset:32
	global_load_dwordx4 v[152:155], v[188:189], off offset:48
	s_ashr_i32 s101, s50, 31
	s_mov_b32 s100, s50
	s_lshl_b64 s[100:101], s[100:101], 8
	v_mov_b32_e32 v195, s101
	v_or_b32_e32 v194, s100, v14
	s_lshl_b32 s98, s3, 1
	s_mov_b32 s99, 0
	v_lshl_add_u64 v[198:199], v[194:195], 0, s[28:29]
	v_lshl_add_u64 v[194:195], v[194:195], 0, s[30:31]
	v_lshl_add_u64 v[196:197], v[22:23], 0, s[98:99]
	v_lshlrev_b64 v[198:199], 14, v[198:199]
	v_lshlrev_b64 v[194:195], 14, v[194:195]
	v_lshl_add_u64 v[190:191], v[196:197], 0, v[198:199]
	v_lshl_add_u64 v[192:193], v[196:197], 0, v[194:195]
	global_load_dwordx4 v[156:159], v[190:191], off
	global_load_dwordx4 v[160:163], v[190:191], off offset:64
	global_load_dwordx4 v[164:167], v[192:193], off
	global_load_dwordx4 v[168:171], v[192:193], off offset:64
	global_load_dwordx4 v[172:175], v[190:191], off offset:128
	global_load_dwordx4 v[176:179], v[192:193], off offset:128
	global_load_dwordx4 v[180:183], v[192:193], off offset:192
	global_load_dwordx4 v[184:187], v[190:191], off offset:192
	s_cbranch_vccnz .LBB0_481
	v_mov_b32_e32 v3, s55
	v_or_b32_e32 v2, s54, v16
	v_lshlrev_b64 v[2:3], 6, v[2:3]
	v_lshl_add_u64 v[2:3], s[22:23], 0, v[2:3]
	s_ashr_i32 s53, s52, 31
	v_lshl_add_u64 v[4:5], s[52:53], 2, v[2:3]
	global_load_dword v7, v[4:5], off offset:88
	global_load_dword v8, v[4:5], off offset:24
	global_load_dword v3, v[4:5], off offset:64
	global_load_dword v2, v[4:5], off
	v_cmp_lt_i32_e32 vcc, v42, v41
	s_waitcnt vmcnt(3)
	v_mul_f32_e64 v10, |v7|, s43
	s_waitcnt vmcnt(2)
	v_mul_f32_e64 v5, |v8|, s43
	v_fma_f32 v11, |v8|, s43, -v5
	v_rndne_f32_e32 v12, v5
	v_fma_f32 v13, |v7|, s43, -v10
	v_rndne_f32_e32 v33, v10
	v_fma_f32 v11, |v8|, s45, v11
	v_sub_f32_e32 v5, v5, v12
	v_fma_f32 v13, |v7|, s45, v13
	v_sub_f32_e32 v10, v10, v33
	v_add_f32_e32 v5, v5, v11
	v_cvt_i32_f32_e32 v12, v12
	v_add_f32_e32 v10, v10, v13
	v_exp_f32_e32 v11, v5
	v_cvt_i32_f32_e32 v33, v33
	v_exp_f32_e32 v10, v10
	v_max_f32_e32 v9, v7, v7
	v_cndmask_b32_e32 v4, v42, v40, vcc
	v_min_f32_e32 v5, 0, v9
	v_ldexp_f32 v9, v11, v12
	v_cmp_ngt_f32_e64 vcc, |v8|, s47
	v_ldexp_f32 v10, v10, v33
	v_lshlrev_b32_e32 v6, 2, v4
	v_cndmask_b32_e32 v9, 0, v9, vcc
	v_cmp_ngt_f32_e64 vcc, |v7|, s47
	v_max_f32_e32 v4, v8, v8
	v_min_f32_e32 v4, 0, v4
	v_cndmask_b32_e32 v10, 0, v10, vcc
	v_cmp_nlt_f32_e64 vcc, |v8|, s58
	s_nop 1
	v_cndmask_b32_e32 v76, v39, v9, vcc
	v_cmp_nlt_f32_e64 vcc, |v7|, s58
	v_add_f32_e32 v12, 1.0, v76
	v_add_f32_e32 v33, -1.0, v12
	v_cndmask_b32_e32 v7, v39, v10, vcc
	v_add_f32_e32 v13, 1.0, v7
	v_frexp_mant_f32_e32 v56, v13
	v_cvt_f64_f32_e32 v[10:11], v13
	v_frexp_exp_i32_f64_e32 v10, v[10:11]
	v_cmp_gt_f32_e32 vcc, s60, v56
	v_frexp_mant_f32_e32 v34, v12
	v_cvt_f64_f32_e32 v[8:9], v12
	v_add_f32_e32 v35, -1.0, v13
	v_subbrev_co_u32_e32 v10, vcc, 0, v10, vcc
	v_sub_f32_e32 v57, v33, v12
	v_frexp_exp_i32_f64_e32 v8, v[8:9]
	v_sub_f32_e32 v9, v35, v13
	v_cmp_gt_f32_e32 vcc, s60, v34
	v_sub_f32_e32 v33, v76, v33
	v_sub_f32_e32 v35, v7, v35
	v_add_f32_e32 v11, 1.0, v57
	v_add_f32_e32 v9, 1.0, v9
	v_subbrev_co_u32_e32 v8, vcc, 0, v8, vcc
	v_add_f32_e32 v11, v33, v11
	v_add_f32_e32 v33, v35, v9
	v_sub_u32_e32 v34, 0, v8
	v_sub_u32_e32 v35, 0, v10
	v_cvt_f32_i32_e32 v9, v10
	v_cvt_f32_i32_e32 v8, v8
	v_ldexp_f32 v10, v12, v34
	v_ldexp_f32 v12, v11, v34
	v_ldexp_f32 v11, v13, v35
	v_ldexp_f32 v13, v33, v35
	v_pk_add_f32 v[34:35], v[10:11], 1.0 op_sel_hi:[1,0]
	v_pk_add_f32 v[56:57], v[10:11], -1.0 op_sel_hi:[1,0]
	v_pk_add_f32 v[58:59], v[34:35], -1.0 op_sel_hi:[1,0]
	v_pk_add_f32 v[60:61], v[56:57], 1.0 op_sel_hi:[1,0]
	v_pk_add_f32 v[58:59], v[10:11], v[58:59] neg_lo:[0,1] neg_hi:[0,1]
	v_pk_add_f32 v[10:11], v[10:11], v[60:61] neg_lo:[0,1] neg_hi:[0,1]
	v_pk_mul_f32 v[60:61], v[8:9], s[44:45] op_sel_hi:[1,0]
	v_pk_add_f32 v[58:59], v[12:13], v[58:59]
	v_pk_add_f32 v[10:11], v[12:13], v[10:11]
	v_pk_fma_f32 v[12:13], v[8:9], s[44:45], v[60:61] op_sel_hi:[1,0,1] neg_lo:[0,0,1] neg_hi:[0,0,1]
	v_pk_add_f32 v[64:65], v[34:35], v[58:59]
	v_mov_b32_e32 v62, v8
	v_pk_fma_f32 v[8:9], v[8:9], s[46:47], v[12:13] op_sel_hi:[1,0,1]
	v_rcp_f32_e32 v12, v64
	v_rcp_f32_e32 v13, v65
	v_pk_add_f32 v[66:67], v[56:57], v[10:11]
	v_pk_add_f32 v[34:35], v[34:35], v[64:65] neg_lo:[0,1] neg_hi:[0,1]
	v_pk_add_f32 v[56:57], v[56:57], v[66:67] neg_lo:[0,1] neg_hi:[0,1]
	v_pk_add_f32 v[34:35], v[58:59], v[34:35]
	v_pk_add_f32 v[10:11], v[10:11], v[56:57]
	v_pk_mul_f32 v[56:57], v[66:67], v[12:13]
	v_cmp_neq_f32_e32 vcc, s59, v76
	v_pk_mul_f32 v[58:59], v[64:65], v[56:57]
	s_nop 0
	v_pk_fma_f32 v[68:69], v[56:57], v[64:65], v[58:59] neg_lo:[0,0,1] neg_hi:[0,0,1]
	s_nop 0
	v_pk_fma_f32 v[68:69], v[56:57], v[34:35], v[68:69]
	s_nop 0
	v_pk_add_f32 v[70:71], v[58:59], v[68:69]
	s_nop 0
	v_pk_add_f32 v[72:73], v[66:67], v[70:71] neg_lo:[0,1] neg_hi:[0,1]
	v_pk_add_f32 v[58:59], v[70:71], v[58:59] neg_lo:[0,1] neg_hi:[0,1]
	v_pk_add_f32 v[66:67], v[66:67], v[72:73] neg_lo:[0,1] neg_hi:[0,1]
	v_pk_add_f32 v[58:59], v[58:59], v[68:69] neg_lo:[0,1] neg_hi:[0,1]
	v_pk_add_f32 v[66:67], v[66:67], v[70:71] neg_lo:[0,1] neg_hi:[0,1]
	s_nop 0
	v_pk_add_f32 v[10:11], v[10:11], v[66:67]
	s_nop 0
	v_pk_add_f32 v[10:11], v[58:59], v[10:11]
	s_nop 0
	v_pk_add_f32 v[58:59], v[72:73], v[10:11]
	s_nop 0
	v_pk_mul_f32 v[66:67], v[12:13], v[58:59]
	v_pk_add_f32 v[68:69], v[72:73], v[58:59] neg_lo:[0,1] neg_hi:[0,1]
	v_pk_mul_f32 v[72:73], v[64:65], v[66:67]
	v_pk_add_f32 v[70:71], v[56:57], v[66:67]
	v_pk_fma_f32 v[64:65], v[66:67], v[64:65], v[72:73] neg_lo:[0,0,1] neg_hi:[0,0,1]
	v_pk_add_f32 v[10:11], v[10:11], v[68:69]
	v_pk_fma_f32 v[34:35], v[66:67], v[34:35], v[64:65]
	v_pk_add_f32 v[56:57], v[70:71], v[56:57] neg_lo:[0,1] neg_hi:[0,1]
	v_pk_add_f32 v[64:65], v[72:73], v[34:35]
	v_pk_add_f32 v[56:57], v[66:67], v[56:57] neg_lo:[0,1] neg_hi:[0,1]
	v_pk_add_f32 v[68:69], v[58:59], v[64:65] neg_lo:[0,1] neg_hi:[0,1]
	v_pk_add_f32 v[66:67], v[64:65], v[72:73] neg_lo:[0,1] neg_hi:[0,1]
	v_pk_add_f32 v[58:59], v[58:59], v[68:69] neg_lo:[0,1] neg_hi:[0,1]
	v_pk_add_f32 v[34:35], v[66:67], v[34:35] neg_lo:[0,1] neg_hi:[0,1]
	v_pk_add_f32 v[58:59], v[58:59], v[64:65] neg_lo:[0,1] neg_hi:[0,1]
	v_mov_b32_e32 v67, v61
	v_pk_add_f32 v[10:11], v[10:11], v[58:59]
	s_nop 0
	v_pk_add_f32 v[10:11], v[34:35], v[10:11]
	s_nop 0
	v_pk_add_f32 v[10:11], v[68:69], v[10:11]
	v_mov_b32_e32 v69, v9
	v_pk_mul_f32 v[10:11], v[12:13], v[10:11]
	s_nop 0
	v_pk_add_f32 v[10:11], v[56:57], v[10:11]
	s_nop 0
	v_pk_add_f32 v[12:13], v[70:71], v[10:11]
	s_nop 0
	v_pk_add_f32 v[34:35], v[12:13], v[70:71] neg_lo:[0,1] neg_hi:[0,1]
	v_pk_mul_f32 v[58:59], v[12:13], v[12:13]
	v_pk_add_f32 v[10:11], v[10:11], v[34:35] neg_lo:[0,1] neg_hi:[0,1]
	v_pk_fma_f32 v[34:35], v[58:59], s[40:41], v[30:31] op_sel_hi:[1,0,0]
	v_pk_mul_f32 v[64:65], v[12:13], v[58:59]
	v_pk_fma_f32 v[34:35], v[58:59], v[34:35], s[42:43] op_sel_hi:[1,1,0]
	v_ldexp_f32 v56, v12, 1
	v_mov_b32_e32 v63, v65
	v_mov_b32_e32 v33, v35
	v_ldexp_f32 v57, v13, 1
	v_pk_mul_f32 v[34:35], v[64:65], v[34:35]
	v_pk_mul_f32 v[58:59], v[62:63], v[32:33]
	v_pk_add_f32 v[62:63], v[56:57], v[34:35]
	v_mov_b32_e32 v65, v57
	v_pk_add_f32 v[56:57], v[62:63], v[56:57] neg_lo:[0,1] neg_hi:[0,1]
	v_ldexp_f32 v10, v10, 1
	v_ldexp_f32 v11, v11, 1
	v_pk_add_f32 v[34:35], v[34:35], v[56:57] neg_lo:[0,1] neg_hi:[0,1]
	v_mov_b32_e32 v64, v8
	v_pk_add_f32 v[56:57], v[10:11], v[34:35]
	v_mov_b32_e32 v34, v60
	v_mov_b32_e32 v10, v8
	v_pk_add_f32 v[58:59], v[58:59], v[64:65]
	v_pk_add_f32 v[64:65], v[34:35], v[10:11]
	v_mov_b32_e32 v10, v62
	v_mov_b32_e32 v34, v56
	v_pk_add_f32 v[12:13], v[60:61], v[8:9]
	v_pk_add_f32 v[10:11], v[10:11], v[34:35]
	v_pk_add_f32 v[34:35], v[62:63], v[56:57]
	v_mov_b32_e32 v66, v12
	v_mov_b32_e32 v68, v34
	v_pk_add_f32 v[10:11], v[58:59], v[10:11]
	v_pk_add_f32 v[58:59], v[12:13], v[34:35]
	v_pk_add_f32 v[70:71], v[66:67], v[68:69]
	v_mov_b32_e32 v72, v34
	v_mov_b32_e32 v73, v59
	v_mov_b32_e32 v74, v62
	v_mov_b32_e32 v75, v13
	v_pk_add_f32 v[66:67], v[70:71], v[66:67] neg_lo:[0,1] neg_hi:[0,1]
	v_pk_add_f32 v[72:73], v[72:73], v[74:75] neg_lo:[0,1] neg_hi:[0,1]
	v_pk_add_f32 v[70:71], v[12:13], v[60:61] neg_lo:[0,1] neg_hi:[0,1]
	v_pk_add_f32 v[68:69], v[68:69], v[66:67] neg_lo:[0,1] neg_hi:[0,1]
	v_mov_b32_e32 v74, v12
	v_mov_b32_e32 v75, v59
	v_mov_b32_e32 v61, v73
	v_mov_b32_e32 v67, v63
	v_pk_add_f32 v[62:63], v[34:35], v[62:63] neg_lo:[0,1] neg_hi:[0,1]
	v_pk_add_f32 v[60:61], v[74:75], v[60:61] neg_lo:[0,1] neg_hi:[0,1]
	v_pk_add_f32 v[70:71], v[8:9], v[70:71] neg_lo:[0,1] neg_hi:[0,1]
	v_pk_add_f32 v[10:11], v[10:11], v[66:67] neg_lo:[0,1] neg_hi:[0,1]
	v_pk_add_f32 v[62:63], v[56:57], v[62:63] neg_lo:[0,1] neg_hi:[0,1]
	v_mov_b32_e32 v9, v13
	v_mov_b32_e32 v57, v35
	v_pk_add_f32 v[10:11], v[64:65], v[10:11] neg_lo:[0,1] neg_hi:[0,1]
	v_pk_add_f32 v[8:9], v[8:9], v[60:61] neg_lo:[0,1] neg_hi:[0,1]
	v_pk_add_f32 v[12:13], v[56:57], v[72:73] neg_lo:[0,1] neg_hi:[0,1]
	v_pk_add_f32 v[56:57], v[68:69], v[10:11]
	v_pk_add_f32 v[34:35], v[12:13], v[8:9]
	v_mov_b32_e32 v13, v11
	v_pk_add_f32 v[10:11], v[70:71], v[12:13]
	v_mov_b32_e32 v9, v69
	v_pk_add_f32 v[10:11], v[10:11], v[8:9] neg_lo:[0,1] neg_hi:[0,1]
	v_mov_b32_e32 v12, v34
	v_mov_b32_e32 v13, v57
	v_pk_add_f32 v[12:13], v[12:13], v[10:11] neg_lo:[0,1] neg_hi:[0,1]
	v_pk_add_f32 v[10:11], v[62:63], v[10:11] neg_lo:[0,1] neg_hi:[0,1]
	v_pk_add_f32 v[8:9], v[8:9], v[12:13] neg_lo:[0,1] neg_hi:[0,1]
	s_nop 0
	v_pk_add_f32 v[8:9], v[10:11], v[8:9]
	v_pk_add_f32 v[10:11], v[56:57], v[34:35]
	s_nop 0
	v_pk_add_f32 v[12:13], v[58:59], v[10:11]
	s_nop 0
	v_pk_add_f32 v[34:35], v[12:13], v[58:59] neg_lo:[0,1] neg_hi:[0,1]
	s_nop 0
	v_pk_add_f32 v[10:11], v[10:11], v[34:35] neg_lo:[0,1] neg_hi:[0,1]
	s_nop 0
	v_pk_add_f32 v[8:9], v[8:9], v[10:11]
	s_nop 0
	v_pk_add_f32 v[8:9], v[12:13], v[8:9]
	s_nop 0
	v_cndmask_b32_e32 v8, v39, v8, vcc
	v_cmp_neq_f32_e32 vcc, s59, v7
	s_nop 1
	v_cndmask_b32_e32 v9, v39, v9, vcc
	v_cmp_lt_f32_e64 vcc, |v7|, s61
	s_nop 1
	v_cndmask_b32_e32 v9, v9, v7, vcc
	v_cmp_lt_f32_e64 vcc, |v76|, s61
	s_nop 1
	v_cndmask_b32_e32 v8, v8, v76, vcc
	v_pk_add_f32 v[4:5], v[4:5], v[8:9] neg_lo:[0,1] neg_hi:[0,1]
	v_cmp_lt_i32_e32 vcc, v43, v41
	v_pk_add_f32 v[34:35], v[4:5], v[4:5] op_sel:[0,1] op_sel_hi:[1,0]
	ds_bpermute_b32 v5, v6, v34
	v_cndmask_b32_e32 v7, v43, v40, vcc
	v_lshlrev_b32_e32 v9, 2, v7
	v_cmp_lt_i32_e32 vcc, v44, v41
	s_waitcnt lgkmcnt(0)
	v_add_f32_e32 v5, v34, v5
	v_cndmask_b32_e64 v5, v5, v34, s[4:5]
	ds_bpermute_b32 v7, v9, v5
	v_cndmask_b32_e32 v8, v44, v40, vcc
	v_lshlrev_b32_e32 v10, 2, v8
	v_cmp_lt_i32_e32 vcc, v45, v41
	s_waitcnt lgkmcnt(0)
	v_add_f32_e32 v7, v5, v7
	v_cndmask_b32_e64 v5, v7, v5, s[6:7]
	ds_bpermute_b32 v7, v10, v5
	v_cndmask_b32_e32 v8, v45, v40, vcc
	v_lshlrev_b32_e32 v11, 2, v8
	v_cmp_lt_i32_e32 vcc, v46, v41
	s_waitcnt lgkmcnt(0)
	v_add_f32_e32 v7, v5, v7
	v_cndmask_b32_e64 v5, v7, v5, s[8:9]
	ds_bpermute_b32 v7, v11, v5
	v_cndmask_b32_e32 v8, v46, v40, vcc
	v_lshlrev_b32_e32 v8, 2, v8
	v_cmp_lt_i32_e32 vcc, v47, v41
	s_waitcnt lgkmcnt(0)
	v_add_f32_e32 v7, v5, v7
	v_cndmask_b32_e64 v5, v7, v5, s[10:11]
	ds_bpermute_b32 v12, v8, v5
	v_cndmask_b32_e32 v7, v47, v40, vcc
	v_lshlrev_b32_e32 v7, 2, v7
	v_cmp_lt_i32_e32 vcc, v50, v49
	s_waitcnt lgkmcnt(0)
	v_add_f32_e32 v12, v5, v12
	v_cndmask_b32_e64 v5, v12, v5, s[12:13]
	ds_bpermute_b32 v12, v7, v5
	s_waitcnt lgkmcnt(0)
	v_add_f32_e32 v12, v5, v12
	v_cndmask_b32_e64 v5, v12, v5, s[14:15]
	ds_bpermute_b32 v12, v48, v5
	v_sub_f32_e32 v5, v5, v34
	v_pk_mov_b32 v[34:35], v[4:5], v[34:35] op_sel:[1,0]
	s_nop 0
	v_pk_add_f32 v[4:5], v[4:5], v[34:35]
	v_cndmask_b32_e32 v35, v40, v50, vcc
	s_waitcnt lgkmcnt(0)
	v_sub_f32_e32 v13, v12, v4
	s_waitcnt vmcnt(0)
	v_add_f32_e32 v33, v2, v13
	v_sub_f32_e32 v13, v12, v5
	v_add_f32_e32 v34, v3, v13
	v_max_f32_e32 v13, v33, v34
	v_lshlrev_b32_e32 v35, 2, v35
	ds_bpermute_b32 v35, v35, v13
	v_cmp_lt_i32_e32 vcc, v51, v49
	s_waitcnt lgkmcnt(0)
	v_max_f32_e32 v35, v35, v35
	v_max_f32_e32 v13, v13, v35
	v_cndmask_b32_e32 v35, v40, v51, vcc
	v_lshlrev_b32_e32 v35, 2, v35
	ds_bpermute_b32 v35, v35, v13
	v_cmp_lt_i32_e32 vcc, v52, v49
	s_waitcnt lgkmcnt(0)
	v_max_f32_e32 v35, v35, v35
	v_max_f32_e32 v13, v13, v35
	v_cndmask_b32_e32 v35, v40, v52, vcc
	v_lshlrev_b32_e32 v35, 2, v35
	ds_bpermute_b32 v35, v35, v13
	v_cmp_lt_i32_e32 vcc, v53, v49
	s_waitcnt lgkmcnt(0)
	v_max_f32_e32 v35, v35, v35
	v_max_f32_e32 v13, v13, v35
	v_cndmask_b32_e32 v35, v40, v53, vcc
	v_lshlrev_b32_e32 v35, 2, v35
	ds_bpermute_b32 v35, v35, v13
	v_cmp_lt_i32_e32 vcc, v54, v49
	s_waitcnt lgkmcnt(0)
	v_max_f32_e32 v35, v35, v35
	v_max_f32_e32 v13, v13, v35
	v_cndmask_b32_e32 v35, v40, v54, vcc
	v_lshlrev_b32_e32 v35, 2, v35
	ds_bpermute_b32 v35, v35, v13
	v_cmp_lt_i32_e32 vcc, v55, v49
	s_waitcnt lgkmcnt(0)
	v_max_f32_e32 v35, v35, v35
	v_max_f32_e32 v13, v13, v35
	v_cndmask_b32_e32 v35, v40, v55, vcc
	v_lshlrev_b32_e32 v35, 2, v35
	ds_bpermute_b32 v35, v35, v13
	s_waitcnt lgkmcnt(0)
	v_max_f32_e32 v35, v35, v35
	v_max_f32_e32 v13, v13, v35
	v_sub_f32_e32 v33, v33, v13
	v_mul_f32_e32 v35, 0x3fb8aa3b, v33
	v_fma_f32 v56, v33, s62, -v35
	v_rndne_f32_e32 v57, v35
	v_fmac_f32_e32 v56, 0x32a5705f, v33
	v_sub_f32_e32 v35, v35, v57
	v_add_f32_e32 v35, v35, v56
	v_exp_f32_e32 v35, v35
	v_cvt_i32_f32_e32 v56, v57
	v_cmp_ngt_f32_e32 vcc, s63, v33
	v_ldexp_f32 v35, v35, v56
	v_sub_f32_e32 v56, v34, v13
	v_mul_f32_e32 v34, 0x3fb8aa3b, v56
	v_fma_f32 v57, v56, s62, -v34
	v_rndne_f32_e32 v58, v34
	v_fmac_f32_e32 v57, 0x32a5705f, v56
	v_sub_f32_e32 v34, v34, v58
	v_add_f32_e32 v34, v34, v57
	v_exp_f32_e32 v57, v34
	v_cvt_i32_f32_e32 v58, v58
	v_cndmask_b32_e32 v34, 0, v35, vcc
	v_cmp_nlt_f32_e32 vcc, s64, v33
	v_ldexp_f32 v33, v57, v58
	s_nop 0
	v_cndmask_b32_e32 v34, v39, v34, vcc
	v_cmp_ngt_f32_e32 vcc, s63, v56
	s_nop 1
	v_cndmask_b32_e32 v33, 0, v33, vcc
	v_cmp_nlt_f32_e32 vcc, s64, v56
	s_nop 1
	v_cndmask_b32_e32 v35, v39, v33, vcc
	ds_write_b64 v1, v[34:35] offset:34816
	s_and_saveexec_b64 s[56:57], s[4:5]
	s_cbranch_execz .LBB0_480
	s_add_u32 s66, s82, s34
	s_addc_u32 s67, s83, s35
	global_store_dword v17, v12, s[66:67]
	global_store_dword v31, v13, s[66:67] offset:2048

.LBB0_481:
	v_lshl_add_u64 v[2:3], s[54:55], 0, v[20:21]
	v_mov_b64_e32 v[4:5], s[24:25]
	v_mad_u64_u32 v[4:5], s[54:55], v2, s65, v[4:5]
	v_mov_b32_e32 v2, v5
	v_mad_u64_u32 v[2:3], s[54:55], v3, s65, v[2:3]
	s_lshl_b32 s52, s52, 7
	v_mov_b32_e32 v5, v2
	s_ashr_i32 s53, s52, 31
	v_lshl_add_u64 v[2:3], s[52:53], 1, v[4:5]
	v_lshl_add_u64 v[34:35], v[2:3], 0, v[18:19]
	s_barrier
	ds_read_b32 v34, v15 offset:34816
	s_waitcnt vmcnt(8)
	v_mov_b32_e32 v2, v140
	v_mov_b32_e32 v3, v141
	v_mov_b32_e32 v4, v142
	v_mov_b32_e32 v5, v143
	v_mov_b32_e32 v6, v144
	v_mov_b32_e32 v7, v145
	v_mov_b32_e32 v8, v146
	v_mov_b32_e32 v9, v147
	v_mov_b32_e32 v10, v148
	v_mov_b32_e32 v11, v149
	v_mov_b32_e32 v12, v150
	v_mov_b32_e32 v13, v151
	v_mov_b32_e32 v56, v152
	v_mov_b32_e32 v57, v153
	v_mov_b32_e32 v58, v154
	v_mov_b32_e32 v59, v155
	v_lshlrev_b32_e32 v60, 16, v2
	v_and_b32_e32 v61, 0xffff0000, v2
	v_lshlrev_b32_e32 v2, 16, v3
	v_and_b32_e32 v3, 0xffff0000, v3
	v_lshlrev_b32_e32 v62, 16, v4
	v_and_b32_e32 v63, 0xffff0000, v4
	v_lshlrev_b32_e32 v4, 16, v5
	v_and_b32_e32 v5, 0xffff0000, v5
	v_lshlrev_b32_e32 v64, 16, v6
	v_and_b32_e32 v65, 0xffff0000, v6
	v_lshlrev_b32_e32 v6, 16, v7
	v_and_b32_e32 v7, 0xffff0000, v7
	v_lshlrev_b32_e32 v66, 16, v8
	v_and_b32_e32 v67, 0xffff0000, v8
	v_lshlrev_b32_e32 v8, 16, v9
	v_and_b32_e32 v9, 0xffff0000, v9
	v_lshlrev_b32_e32 v68, 16, v10
	v_and_b32_e32 v69, 0xffff0000, v10
	v_lshlrev_b32_e32 v10, 16, v11
	v_and_b32_e32 v11, 0xffff0000, v11
	v_lshlrev_b32_e32 v70, 16, v12
	v_and_b32_e32 v71, 0xffff0000, v12
	v_lshlrev_b32_e32 v12, 16, v13
	v_and_b32_e32 v13, 0xffff0000, v13
	s_waitcnt lgkmcnt(0)
	v_pk_mul_f32 v[60:61], v[34:35], v[60:61] op_sel_hi:[0,1]
	v_pk_mul_f32 v[2:3], v[34:35], v[2:3] op_sel_hi:[0,1]
	v_pk_mul_f32 v[62:63], v[34:35], v[62:63] op_sel_hi:[0,1]
	v_pk_mul_f32 v[4:5], v[34:35], v[4:5] op_sel_hi:[0,1]
	v_pk_mul_f32 v[64:65], v[34:35], v[64:65] op_sel_hi:[0,1]
	v_pk_mul_f32 v[6:7], v[34:35], v[6:7] op_sel_hi:[0,1]
	v_pk_mul_f32 v[66:67], v[34:35], v[66:67] op_sel_hi:[0,1]
	v_pk_mul_f32 v[8:9], v[34:35], v[8:9] op_sel_hi:[0,1]
	v_pk_mul_f32 v[68:69], v[34:35], v[68:69] op_sel_hi:[0,1]
	v_pk_mul_f32 v[10:11], v[34:35], v[10:11] op_sel_hi:[0,1]
	v_pk_mul_f32 v[70:71], v[34:35], v[70:71] op_sel_hi:[0,1]
	v_pk_mul_f32 v[12:13], v[34:35], v[12:13] op_sel_hi:[0,1]
	v_cvt_pk_bf16_f32 v33, v60, v61
	v_cvt_pk_bf16_f32 v2, v2, v3
	v_cvt_pk_bf16_f32 v3, v62, v63
	v_cvt_pk_bf16_f32 v4, v4, v5
	v_cvt_pk_bf16_f32 v5, v64, v65
	v_cvt_pk_bf16_f32 v6, v6, v7
	v_cvt_pk_bf16_f32 v7, v66, v67
	v_cvt_pk_bf16_f32 v8, v8, v9
	v_cvt_pk_bf16_f32 v9, v68, v69
	v_cvt_pk_bf16_f32 v10, v10, v11
	v_cvt_pk_bf16_f32 v11, v70, v71
	v_cvt_pk_bf16_f32 v12, v12, v13
	ds_write_b16 v36, v33
	ds_write_b16_d16_hi v36, v33 offset:272
	ds_write_b16 v36, v2 offset:544
	ds_write_b16_d16_hi v36, v2 offset:816
	ds_write_b16 v36, v3 offset:1088
	ds_write_b16_d16_hi v36, v3 offset:1360
	ds_write_b16 v36, v4 offset:1632
	ds_write_b16_d16_hi v36, v4 offset:1904
	ds_write_b16 v36, v5 offset:2176
	ds_write_b16_d16_hi v36, v5 offset:2448
	ds_write_b16 v36, v6 offset:2720
	ds_write_b16_d16_hi v36, v6 offset:2992
	ds_write_b16 v36, v7 offset:3264
	ds_write_b16_d16_hi v36, v7 offset:3536
	ds_write_b16 v36, v8 offset:3808
	ds_write_b16_d16_hi v36, v8 offset:4080
	ds_write_b16 v36, v9 offset:4352
	ds_write_b16_d16_hi v36, v9 offset:4624
	ds_write_b16 v36, v10 offset:4896
	ds_write_b16_d16_hi v36, v10 offset:5168
	ds_write_b16 v36, v11 offset:5440
	ds_write_b16_d16_hi v36, v11 offset:5712
	ds_write_b16 v36, v12 offset:5984
	ds_write_b16_d16_hi v36, v12 offset:6256
	v_lshlrev_b32_e32 v2, 16, v56
	v_and_b32_e32 v3, 0xffff0000, v56
	v_pk_mul_f32 v[2:3], v[34:35], v[2:3] op_sel_hi:[0,1]
	v_cvt_pk_bf16_f32 v2, v2, v3
	ds_write_b16 v36, v2 offset:6528
	ds_write_b16_d16_hi v36, v2 offset:6800
	v_lshlrev_b32_e32 v2, 16, v57
	v_and_b32_e32 v3, 0xffff0000, v57
	v_pk_mul_f32 v[2:3], v[34:35], v[2:3] op_sel_hi:[0,1]
	v_cvt_pk_bf16_f32 v2, v2, v3
	ds_write_b16 v36, v2 offset:7072
	ds_write_b16_d16_hi v36, v2 offset:7344
	v_lshlrev_b32_e32 v2, 16, v58
	v_and_b32_e32 v3, 0xffff0000, v58
	v_pk_mul_f32 v[2:3], v[34:35], v[2:3] op_sel_hi:[0,1]
	v_cvt_pk_bf16_f32 v2, v2, v3
	ds_write_b16 v36, v2 offset:7616
	ds_write_b16_d16_hi v36, v2 offset:7888
	v_lshlrev_b32_e32 v2, 16, v59
	v_and_b32_e32 v3, 0xffff0000, v59
	v_pk_mul_f32 v[2:3], v[34:35], v[2:3] op_sel_hi:[0,1]
	v_cvt_pk_bf16_f32 v2, v2, v3
	ds_write_b16 v36, v2 offset:8160
	ds_write_b16_d16_hi v36, v2 offset:8432
	s_waitcnt lgkmcnt(0)
	s_barrier
	s_and_saveexec_b64 s[52:53], s[16:17]
	s_xor_b64 s[52:53], exec, s[52:53]
	s_ashr_i32 s55, s48, 31
	s_mov_b32 s54, s48
	s_or_saveexec_b64 s[52:53], s[52:53]
	v_mov_b64_e32 v[34:35], s[54:55]
	s_xor_b64 exec, exec, s[52:53]
	s_cbranch_execz .LBB0_476
	ds_read_b128 v[2:5], v37
	ds_read_b128 v[6:9], v37 offset:16
	ds_read_b128 v[10:13], v37 offset:32
	ds_read_b128 v[56:59], v37 offset:48
	s_waitcnt lgkmcnt(3)
	v_lshlrev_b32_e32 v35, 16, v3
	v_lshlrev_b32_e32 v34, 16, v2
	v_and_b32_e32 v3, 0xffff0000, v3
	v_and_b32_e32 v2, 0xffff0000, v2
	v_pk_add_f32 v[2:3], v[34:35], v[2:3]
	v_lshlrev_b32_e32 v35, 16, v5
	v_lshlrev_b32_e32 v34, 16, v4
	v_and_b32_e32 v5, 0xffff0000, v5
	v_and_b32_e32 v4, 0xffff0000, v4
	v_pk_add_f32 v[4:5], v[34:35], v[4:5]
	v_add_f32_e32 v2, v2, v3
	v_add_f32_e32 v2, v4, v2
	v_add_f32_e32 v2, v5, v2
	v_add_f32_e32 v34, 0, v2
	s_waitcnt lgkmcnt(2)
	v_lshlrev_b32_e32 v3, 16, v7
	v_lshlrev_b32_e32 v2, 16, v6
	v_and_b32_e32 v5, 0xffff0000, v7
	v_and_b32_e32 v4, 0xffff0000, v6
	v_pk_add_f32 v[2:3], v[2:3], v[4:5]
	v_lshlrev_b32_e32 v5, 16, v9
	v_lshlrev_b32_e32 v4, 16, v8
	v_and_b32_e32 v7, 0xffff0000, v9
	v_and_b32_e32 v6, 0xffff0000, v8
	v_pk_add_f32 v[4:5], v[4:5], v[6:7]
	s_waitcnt lgkmcnt(1)
	v_lshlrev_b32_e32 v6, 16, v10
	v_and_b32_e32 v7, 0xffff0000, v10
	v_add_f32_e32 v6, v6, v7
	v_lshlrev_b32_e32 v7, 16, v11
	v_and_b32_e32 v8, 0xffff0000, v11
	v_add_f32_e32 v8, v7, v8
	s_waitcnt lgkmcnt(0)
	v_lshlrev_b32_e32 v7, 16, v57
	v_and_b32_e32 v9, 0xffff0000, v57
	v_lshlrev_b32_e32 v11, 16, v56
	v_lshlrev_b32_e32 v10, 16, v12
	v_and_b32_e32 v57, 0xffff0000, v56
	v_and_b32_e32 v56, 0xffff0000, v12
	v_pk_add_f32 v[10:11], v[10:11], v[56:57]
	v_pk_add_f32 v[6:7], v[6:7], v[8:9]
	v_pk_mov_b32 v[8:9], v[12:13], v[58:59] op_sel:[1,0]
	v_pk_add_f32 v[2:3], v[2:3], v[2:3] op_sel:[0,1] op_sel_hi:[1,0]
	v_pk_add_f32 v[6:7], v[10:11], v[6:7]
	v_lshlrev_b32_e32 v11, 16, v58
	v_lshlrev_b32_e32 v10, 16, v13
	v_and_b32_e32 v9, 0xffff0000, v9
	v_and_b32_e32 v8, 0xffff0000, v8
	v_pk_add_f32 v[2:3], v[4:5], v[2:3]
	v_pk_add_f32 v[8:9], v[10:11], v[8:9]
	v_and_b32_e32 v33, 0xffff0000, v59
	v_pk_add_f32 v[6:7], v[8:9], v[6:7]
	v_pk_add_f32 v[8:9], v[4:5], v[2:3] op_sel:[1,0] op_sel_hi:[0,1]
	ds_read_b128 v[2:5], v37 offset:64
	v_lshlrev_b32_e32 v35, 16, v59
	v_mov_b32_e32 v9, v33
	v_pk_add_f32 v[8:9], v[34:35], v[8:9]
	s_nop 0
	v_pk_add_f32 v[34:35], v[8:9], v[6:7]
	ds_read_b128 v[6:9], v37 offset:80
	s_waitcnt lgkmcnt(1)
	v_lshlrev_b32_e32 v11, 16, v3
	v_lshlrev_b32_e32 v10, 16, v2
	v_and_b32_e32 v3, 0xffff0000, v3
	v_and_b32_e32 v2, 0xffff0000, v2
	v_pk_add_f32 v[2:3], v[10:11], v[2:3]
	v_lshlrev_b32_e32 v11, 16, v5
	v_lshlrev_b32_e32 v10, 16, v4
	v_and_b32_e32 v5, 0xffff0000, v5
	v_and_b32_e32 v4, 0xffff0000, v4
	v_pk_add_f32 v[2:3], v[2:3], v[2:3] op_sel:[0,1] op_sel_hi:[1,0]
	v_pk_add_f32 v[56:57], v[10:11], v[4:5]
	s_waitcnt lgkmcnt(0)
	v_lshlrev_b32_e32 v10, 16, v7
	v_pk_add_f32 v[58:59], v[56:57], v[2:3]
	v_lshlrev_b32_e32 v2, 16, v6
	v_and_b32_e32 v3, 0xffff0000, v6
	v_add_f32_e32 v6, v2, v3
	ds_read_b128 v[2:5], v37 offset:96
	v_and_b32_e32 v7, 0xffff0000, v7
	v_add_f32_e32 v60, v10, v7
	ds_read_b128 v[10:13], v37 offset:112
	v_lshlrev_b32_e32 v62, 16, v8
	s_waitcnt lgkmcnt(1)
	v_lshlrev_b32_e32 v7, 16, v3
	v_and_b32_e32 v61, 0xffff0000, v3
	v_lshlrev_b32_e32 v63, 16, v2
	v_and_b32_e32 v3, 0xffff0000, v2
	v_and_b32_e32 v2, 0xffff0000, v8
	v_pk_add_f32 v[2:3], v[62:63], v[2:3]
	v_pk_add_f32 v[6:7], v[6:7], v[60:61]
	v_lshlrev_b32_e32 v33, 16, v5
	v_pk_add_f32 v[2:3], v[2:3], v[6:7]
	v_pk_mov_b32 v[6:7], v[8:9], v[4:5] op_sel:[1,0]
	v_and_b32_e32 v64, 0xffff0000, v5
	v_lshlrev_b32_e32 v5, 16, v4
	v_lshlrev_b32_e32 v4, 16, v9
	v_and_b32_e32 v7, 0xffff0000, v7
	v_and_b32_e32 v6, 0xffff0000, v6
	v_pk_add_f32 v[4:5], v[4:5], v[6:7]
	v_pk_add_f32 v[6:7], v[56:57], v[58:59] op_sel:[1,0] op_sel_hi:[0,1]
	v_pk_add_f32 v[2:3], v[4:5], v[2:3]
	v_pk_add_f32 v[4:5], v[34:35], v[34:35] op_sel:[0,1] op_sel_hi:[1,0]
	v_mov_b32_e32 v7, v64
	v_mov_b32_e32 v5, v33
	v_pk_add_f32 v[4:5], v[4:5], v[6:7]
	s_waitcnt lgkmcnt(0)
	v_lshlrev_b32_e32 v9, 16, v13
	v_pk_add_f32 v[34:35], v[4:5], v[2:3]
	v_lshlrev_b32_e32 v3, 16, v11
	v_lshlrev_b32_e32 v2, 16, v10
	v_and_b32_e32 v5, 0xffff0000, v11
	v_and_b32_e32 v4, 0xffff0000, v10
	v_pk_add_f32 v[2:3], v[2:3], v[4:5]
	v_lshlrev_b32_e32 v8, 16, v12
	v_pk_add_f32 v[6:7], v[2:3], v[2:3] op_sel:[0,1] op_sel_hi:[1,0]
	v_and_b32_e32 v11, 0xffff0000, v13
	ds_read_b128 v[2:5], v37 offset:128
	v_and_b32_e32 v10, 0xffff0000, v12
	v_pk_add_f32 v[10:11], v[8:9], v[10:11]
	s_nop 0
	v_pk_add_f32 v[12:13], v[10:11], v[6:7]
	ds_read_b128 v[6:9], v37 offset:144
	s_waitcnt lgkmcnt(1)
	v_lshlrev_b32_e32 v33, 16, v2
	v_and_b32_e32 v2, 0xffff0000, v2
	v_add_f32_e32 v2, v33, v2
	v_lshlrev_b32_e32 v33, 16, v3
	v_and_b32_e32 v3, 0xffff0000, v3
	v_add_f32_e32 v56, v33, v3
	s_waitcnt lgkmcnt(0)
	v_lshlrev_b32_e32 v3, 16, v7
	v_and_b32_e32 v57, 0xffff0000, v7
	v_lshlrev_b32_e32 v59, 16, v6
	v_lshlrev_b32_e32 v58, 16, v4
	v_and_b32_e32 v7, 0xffff0000, v6
	v_and_b32_e32 v6, 0xffff0000, v4
	v_pk_add_f32 v[6:7], v[58:59], v[6:7]
	v_pk_add_f32 v[2:3], v[2:3], v[56:57]
	v_lshlrev_b32_e32 v33, 16, v9
	v_pk_add_f32 v[2:3], v[6:7], v[2:3]
	v_pk_mov_b32 v[6:7], v[4:5], v[8:9] op_sel:[1,0]
	v_and_b32_e32 v60, 0xffff0000, v9
	v_lshlrev_b32_e32 v9, 16, v8
	v_lshlrev_b32_e32 v8, 16, v5
	v_and_b32_e32 v5, 0xffff0000, v7
	v_and_b32_e32 v4, 0xffff0000, v6
	v_pk_add_f32 v[4:5], v[8:9], v[4:5]
	v_pk_add_f32 v[8:9], v[34:35], v[34:35] op_sel:[0,1] op_sel_hi:[1,0]
	v_pk_add_f32 v[6:7], v[4:5], v[2:3]
	v_pk_add_f32 v[10:11], v[10:11], v[12:13] op_sel:[1,0] op_sel_hi:[0,1]
	ds_read_b128 v[2:5], v37 offset:160
	v_mov_b32_e32 v9, v33
	v_mov_b32_e32 v11, v60
	v_pk_add_f32 v[8:9], v[8:9], v[10:11]
	s_nop 0
	v_pk_add_f32 v[34:35], v[8:9], v[6:7]
	ds_read_b128 v[6:9], v37 offset:176
	s_waitcnt lgkmcnt(1)
	v_lshlrev_b32_e32 v11, 16, v3
	v_lshlrev_b32_e32 v10, 16, v2
	v_and_b32_e32 v3, 0xffff0000, v3
	v_and_b32_e32 v2, 0xffff0000, v2
	v_pk_add_f32 v[2:3], v[10:11], v[2:3]
	v_lshlrev_b32_e32 v11, 16, v5
	v_lshlrev_b32_e32 v10, 16, v4
	v_and_b32_e32 v5, 0xffff0000, v5
	v_and_b32_e32 v4, 0xffff0000, v4
	v_pk_add_f32 v[2:3], v[2:3], v[2:3] op_sel:[0,1] op_sel_hi:[1,0]
	v_pk_add_f32 v[56:57], v[10:11], v[4:5]
	s_waitcnt lgkmcnt(0)
	v_lshlrev_b32_e32 v10, 16, v7
	v_pk_add_f32 v[58:59], v[56:57], v[2:3]
	v_lshlrev_b32_e32 v2, 16, v6
	v_and_b32_e32 v3, 0xffff0000, v6
	v_add_f32_e32 v6, v2, v3
	ds_read_b128 v[2:5], v37 offset:192
	v_and_b32_e32 v7, 0xffff0000, v7
	v_add_f32_e32 v60, v10, v7
	ds_read_b128 v[10:13], v37 offset:208
	v_lshlrev_b32_e32 v62, 16, v8
	s_waitcnt lgkmcnt(1)
	v_lshlrev_b32_e32 v7, 16, v3
	v_and_b32_e32 v61, 0xffff0000, v3
	v_lshlrev_b32_e32 v63, 16, v2
	v_and_b32_e32 v3, 0xffff0000, v2
	v_and_b32_e32 v2, 0xffff0000, v8
	v_pk_add_f32 v[2:3], v[62:63], v[2:3]
	v_pk_add_f32 v[6:7], v[6:7], v[60:61]
	v_lshlrev_b32_e32 v33, 16, v5
	v_pk_add_f32 v[2:3], v[2:3], v[6:7]
	v_pk_mov_b32 v[6:7], v[8:9], v[4:5] op_sel:[1,0]
	v_and_b32_e32 v64, 0xffff0000, v5
	v_lshlrev_b32_e32 v5, 16, v4
	v_lshlrev_b32_e32 v4, 16, v9
	v_and_b32_e32 v7, 0xffff0000, v7
	v_and_b32_e32 v6, 0xffff0000, v6
	v_pk_add_f32 v[4:5], v[4:5], v[6:7]
	v_pk_add_f32 v[6:7], v[56:57], v[58:59] op_sel:[1,0] op_sel_hi:[0,1]
	v_pk_add_f32 v[2:3], v[4:5], v[2:3]
	v_pk_add_f32 v[4:5], v[34:35], v[34:35] op_sel:[0,1] op_sel_hi:[1,0]
	v_mov_b32_e32 v7, v64
	v_mov_b32_e32 v5, v33
	v_pk_add_f32 v[4:5], v[4:5], v[6:7]
	s_waitcnt lgkmcnt(0)
	v_lshlrev_b32_e32 v9, 16, v13
	v_pk_add_f32 v[34:35], v[4:5], v[2:3]
	v_lshlrev_b32_e32 v3, 16, v11
	v_lshlrev_b32_e32 v2, 16, v10
	v_and_b32_e32 v5, 0xffff0000, v11
	v_and_b32_e32 v4, 0xffff0000, v10
	v_pk_add_f32 v[2:3], v[2:3], v[4:5]
	v_lshlrev_b32_e32 v8, 16, v12
	v_pk_add_f32 v[6:7], v[2:3], v[2:3] op_sel:[0,1] op_sel_hi:[1,0]
	v_and_b32_e32 v11, 0xffff0000, v13
	ds_read_b128 v[2:5], v37 offset:224
	v_and_b32_e32 v10, 0xffff0000, v12
	v_pk_add_f32 v[10:11], v[8:9], v[10:11]
	s_nop 0
	v_pk_add_f32 v[12:13], v[10:11], v[6:7]
	ds_read_b128 v[6:9], v37 offset:240
	s_waitcnt lgkmcnt(1)
	v_lshlrev_b32_e32 v33, 16, v2
	v_and_b32_e32 v2, 0xffff0000, v2
	v_add_f32_e32 v2, v33, v2
	v_lshlrev_b32_e32 v33, 16, v3
	v_and_b32_e32 v3, 0xffff0000, v3
	v_add_f32_e32 v56, v33, v3
	s_waitcnt lgkmcnt(0)
	v_lshlrev_b32_e32 v3, 16, v7
	v_and_b32_e32 v57, 0xffff0000, v7
	v_lshlrev_b32_e32 v59, 16, v6
	v_lshlrev_b32_e32 v58, 16, v4
	v_and_b32_e32 v7, 0xffff0000, v6
	v_and_b32_e32 v6, 0xffff0000, v4
	v_pk_add_f32 v[6:7], v[58:59], v[6:7]
	v_pk_add_f32 v[2:3], v[2:3], v[56:57]
	v_lshlrev_b32_e32 v33, 16, v9
	v_pk_add_f32 v[2:3], v[6:7], v[2:3]
	v_pk_mov_b32 v[6:7], v[4:5], v[8:9] op_sel:[1,0]
	v_and_b32_e32 v60, 0xffff0000, v9
	v_lshlrev_b32_e32 v9, 16, v8
	v_lshlrev_b32_e32 v8, 16, v5
	v_and_b32_e32 v5, 0xffff0000, v7
	v_and_b32_e32 v4, 0xffff0000, v6
	v_pk_add_f32 v[4:5], v[8:9], v[4:5]
	v_pk_add_f32 v[6:7], v[10:11], v[12:13] op_sel:[1,0] op_sel_hi:[0,1]
	v_pk_add_f32 v[2:3], v[4:5], v[2:3]
	v_pk_add_f32 v[4:5], v[34:35], v[34:35] op_sel:[0,1] op_sel_hi:[1,0]
	v_mov_b32_e32 v7, v60
	v_mov_b32_e32 v5, v33
	v_pk_add_f32 v[4:5], v[4:5], v[6:7]
	v_mov_b64_e32 v[34:35], s[48:49]
	v_pk_add_f32 v[2:3], v[4:5], v[2:3]
	s_nop 0
	v_add_f32_e32 v4, v2, v3
	v_lshl_add_u64 v[2:3], s[82:83], 0, v[28:29]
	global_store_dword v[2:3], v4, off
	s_branch .LBB0_476

.LBB0_659:
	s_ashr_i32 s70, s39, 6
	s_ashr_i32 s71, s70, 31
	s_and_b32 s74, s33, 0x1f80
	s_lshl_b64 s[30:31], s[70:71], 22
	v_lshl_add_u64 v[50:51], v[162:163], 0, s[30:31]
	s_lshl_b32 s88, s74, 1
	v_lshl_add_u64 v[50:51], v[50:51], 0, s[88:89]
	v_lshl_add_u64 v[94:95], v[50:51], 0, v[160:161]
	global_load_dword v114, v[198:199], off
	global_load_dwordx4 v[50:53], v[94:95], off offset:48
	global_load_dwordx4 v[54:57], v[94:95], off offset:32
	global_load_dwordx4 v[58:61], v[94:95], off offset:16
	global_load_dwordx4 v[62:65], v[94:95], off
	global_load_dwordx4 v[66:69], v[200:201], off offset:-16
	global_load_dwordx4 v[70:73], v[200:201], off offset:-32
	global_load_dwordx4 v[74:77], v[200:201], off offset:-48
	global_load_dwordx4 v[78:81], v[200:201], off offset:-64
	global_load_dwordx4 v[82:85], v[94:95], off offset:112
	global_load_dwordx4 v[86:89], v[94:95], off offset:96
	global_load_dwordx4 v[90:93], v[94:95], off offset:80
	s_nop 0
	global_load_dwordx4 v[94:97], v[94:95], off offset:64
	s_nop 0
	global_load_dwordx4 v[98:101], v[200:201], off offset:48
	global_load_dwordx4 v[102:105], v[200:201], off offset:32
	global_load_dwordx4 v[106:109], v[200:201], off offset:16
	global_load_dwordx4 v[110:113], v[200:201], off
	s_mul_hi_i32 s30, s70, 0x2aaaaaab
	s_lshr_b32 s31, s30, 31
	s_add_i32 s72, s30, s31
	s_ashr_i32 s73, s72, 31
	s_lshl_b64 s[30:31], s[72:73], 13
	s_or_b32 s30, s30, s74
	s_mul_i32 s71, s72, 6
	v_lshl_add_u64 v[204:205], s[30:31], 0, v[164:165]
	v_mov_b64_e32 v[252:253], s[92:93]
	s_sub_i32 s88, s70, s71
	v_mad_u64_u32 v[252:253], s[70:71], v204, s3, v[252:253]
	s_lshl_b32 s70, s88, 7
	s_ashr_i32 s71, s70, 31
	v_mad_i32_i24 v253, v205, s3, v253
	s_lshl_b64 s[70:71], s[70:71], 1
	v_lshl_add_u64 v[252:253], v[252:253], 0, s[70:71]
	v_mov_b32_e32 v203, v161
	v_lshl_add_u64 v[244:245], v[252:253], 0, v[202:203]
	global_load_dwordx4 v[232:235], v[244:245], off
	global_load_dwordx4 v[236:239], v[244:245], off offset:64
	global_load_dwordx4 v[240:243], v[244:245], off offset:128
	global_load_dwordx4 v[248:251], v[244:245], off offset:192
	global_load_dword v210, v161, s[22:23]
	s_waitcnt vmcnt(21)
	ds_write_b32 v1, v114
	s_waitcnt vmcnt(17)
	ds_write_b128 v183, v[62:65]
	s_waitcnt vmcnt(13)
	ds_write_b128 v212, v[78:81]
	ds_write_b128 v183, v[58:61] offset:16
	ds_write_b128 v212, v[74:77] offset:16
	ds_write_b128 v183, v[54:57] offset:32
	ds_write_b128 v212, v[70:73] offset:32
	ds_write_b128 v183, v[50:53] offset:48
	ds_write_b128 v212, v[66:69] offset:48
	s_waitcnt vmcnt(9)
	ds_write_b128 v183, v[94:97] offset:64
	s_waitcnt vmcnt(5)
	ds_write_b128 v212, v[110:113] offset:64
	ds_write_b128 v183, v[90:93] offset:80
	ds_write_b128 v212, v[106:109] offset:80
	ds_write_b128 v183, v[86:89] offset:96
	ds_write_b128 v212, v[102:105] offset:96
	ds_write_b128 v183, v[82:85] offset:112
	ds_write_b128 v212, v[98:101] offset:112
	s_waitcnt lgkmcnt(0)
	s_barrier
	ds_read_b32 v130, v159
	ds_read_b32 v208, v171
	ds_read_b128 v[54:57], v173
	ds_read_b128 v[58:61], v173 offset:16
	v_lshl_add_u64 v[138:139], v[166:167], 0, s[70:71]
	v_or_b32_e32 v131, s30, v158
	s_andn2_b64 vcc, exec, s[94:95]
	ds_read_b128 v[74:77], v213 offset:4416
	ds_read_b128 v[78:81], v213 offset:8768
	ds_read_b128 v[82:85], v213 offset:13120
	s_waitcnt vmcnt(0)
	v_mov_b32_e32 v50, v232
	v_mov_b32_e32 v51, v233
	v_mov_b32_e32 v52, v234
	v_mov_b32_e32 v53, v235
	v_and_b32_e32 v65, 0xffff0000, v50
	v_lshlrev_b32_e32 v64, 16, v50
	s_waitcnt lgkmcnt(4)
	v_mul_f32_e32 v55, v55, v65
	v_fmac_f32_e32 v55, v54, v64
	v_lshlrev_b32_e32 v54, 16, v51
	v_fmac_f32_e32 v55, v56, v54
	v_and_b32_e32 v54, 0xffff0000, v51
	v_fmac_f32_e32 v55, v57, v54
	v_lshlrev_b32_e32 v54, 16, v52
	s_waitcnt lgkmcnt(3)
	v_fmac_f32_e32 v55, v58, v54
	v_and_b32_e32 v54, 0xffff0000, v52
	v_fmac_f32_e32 v55, v59, v54
	v_lshlrev_b32_e32 v54, 16, v53
	v_fmac_f32_e32 v55, v60, v54
	v_and_b32_e32 v54, 0xffff0000, v53
	v_fmac_f32_e32 v55, v61, v54
	v_add_f32_e32 v64, 0, v55
	ds_read_b128 v[58:61], v173 offset:128
	v_mov_b32_e32 v54, v236
	v_mov_b32_e32 v55, v237
	v_mov_b32_e32 v56, v238
	v_mov_b32_e32 v57, v239
	v_and_b32_e32 v66, 0xffff0000, v54
	v_lshlrev_b32_e32 v65, 16, v54
	s_waitcnt lgkmcnt(0)
	v_mul_f32_e32 v66, v59, v66
	v_fmac_f32_e32 v66, v58, v65
	v_lshlrev_b32_e32 v58, 16, v55
	v_fmac_f32_e32 v66, v60, v58
	v_and_b32_e32 v58, 0xffff0000, v55
	v_fmac_f32_e32 v66, v61, v58
	ds_read_b128 v[58:61], v173 offset:144
	v_lshlrev_b32_e32 v65, 16, v56
	s_waitcnt lgkmcnt(0)
	v_fmac_f32_e32 v66, v58, v65
	v_and_b32_e32 v58, 0xffff0000, v56
	v_fmac_f32_e32 v66, v59, v58
	v_lshlrev_b32_e32 v58, 16, v57
	v_fmac_f32_e32 v66, v60, v58
	v_and_b32_e32 v58, 0xffff0000, v57
	v_fmac_f32_e32 v66, v61, v58
	v_add_f32_e32 v68, v64, v66
	ds_read_b128 v[64:67], v173 offset:256
	v_mov_b32_e32 v58, v240
	v_mov_b32_e32 v59, v241
	v_mov_b32_e32 v60, v242
	v_mov_b32_e32 v61, v243
	v_and_b32_e32 v70, 0xffff0000, v58
	v_lshlrev_b32_e32 v69, 16, v58
	s_waitcnt lgkmcnt(0)
	v_mul_f32_e32 v70, v65, v70
	v_fmac_f32_e32 v70, v64, v69
	v_lshlrev_b32_e32 v64, 16, v59
	v_fmac_f32_e32 v70, v66, v64
	v_and_b32_e32 v64, 0xffff0000, v59
	v_fmac_f32_e32 v70, v67, v64
	ds_read_b128 v[64:67], v173 offset:272
	v_lshlrev_b32_e32 v69, 16, v60
	s_waitcnt lgkmcnt(0)
	v_fmac_f32_e32 v70, v64, v69
	v_and_b32_e32 v64, 0xffff0000, v60
	v_fmac_f32_e32 v70, v65, v64
	v_lshlrev_b32_e32 v64, 16, v61
	v_fmac_f32_e32 v70, v66, v64
	v_and_b32_e32 v64, 0xffff0000, v61
	v_fmac_f32_e32 v70, v67, v64
	v_add_f32_e32 v66, v68, v70
	ds_read_b128 v[62:65], v173 offset:384
	v_mov_b32_e32 v70, v248
	v_mov_b32_e32 v71, v249
	v_mov_b32_e32 v72, v250
	v_mov_b32_e32 v73, v251
	v_and_b32_e32 v68, 0xffff0000, v70
	v_lshlrev_b32_e32 v67, 16, v70
	s_waitcnt lgkmcnt(0)
	v_mul_f32_e32 v68, v63, v68
	v_fmac_f32_e32 v68, v62, v67
	v_lshlrev_b32_e32 v62, 16, v71
	v_fmac_f32_e32 v68, v64, v62
	v_and_b32_e32 v62, 0xffff0000, v71
	v_fmac_f32_e32 v68, v65, v62
	ds_read_b128 v[62:65], v173 offset:400
	v_lshlrev_b32_e32 v67, 16, v72
	s_waitcnt lgkmcnt(0)
	v_fmac_f32_e32 v68, v62, v67
	v_and_b32_e32 v62, 0xffff0000, v72
	v_fmac_f32_e32 v68, v63, v62
	v_lshlrev_b32_e32 v62, 16, v73
	v_fmac_f32_e32 v68, v64, v62
	v_and_b32_e32 v62, 0xffff0000, v73
	v_fmac_f32_e32 v68, v65, v62
	v_add_f32_e32 v62, v66, v68
	ds_bpermute_b32 v63, v175, v62
	ds_read_b128 v[66:69], v213 offset:64
	s_waitcnt lgkmcnt(1)
	v_add_f32_e32 v203, v62, v63
	ds_read_b128 v[62:65], v213
	s_waitcnt lgkmcnt(0)
	v_mfma_f32_16x16x32_bf16 v[62:65], v[62:65], v[50:53], 0
	ds_bpermute_b32 v209, v177, v203
	v_mfma_f32_16x16x32_bf16 v[62:65], v[66:69], v[54:57], v[62:65]
	ds_read_b128 v[66:69], v213 offset:128
	s_waitcnt lgkmcnt(0)
	v_mfma_f32_16x16x32_bf16 v[62:65], v[66:69], v[58:61], v[62:65]
	ds_read_b128 v[66:69], v213 offset:192
	s_waitcnt lgkmcnt(0)
	v_mfma_f32_16x16x32_bf16 v[62:65], v[66:69], v[70:73], v[62:65]
	ds_read_b128 v[66:69], v213 offset:4352
	s_waitcnt lgkmcnt(0)
	v_mfma_f32_16x16x32_bf16 v[66:69], v[66:69], v[50:53], 0
	v_mfma_f32_16x16x32_bf16 v[66:69], v[74:77], v[54:57], v[66:69]
	ds_read_b128 v[74:77], v213 offset:4480
	s_waitcnt lgkmcnt(0)
	v_mfma_f32_16x16x32_bf16 v[66:69], v[74:77], v[58:61], v[66:69]
	ds_read_b128 v[74:77], v213 offset:4544
	s_waitcnt lgkmcnt(0)
	v_mfma_f32_16x16x32_bf16 v[66:69], v[74:77], v[70:73], v[66:69]
	ds_read_b128 v[74:77], v213 offset:8704
	s_waitcnt lgkmcnt(0)
	v_mfma_f32_16x16x32_bf16 v[74:77], v[74:77], v[50:53], 0
	v_mfma_f32_16x16x32_bf16 v[74:77], v[78:81], v[54:57], v[74:77]
	ds_read_b128 v[78:81], v213 offset:8832
	s_waitcnt lgkmcnt(0)
	v_mfma_f32_16x16x32_bf16 v[74:77], v[78:81], v[58:61], v[74:77]
	ds_read_b128 v[78:81], v213 offset:8896
	s_waitcnt lgkmcnt(0)
	v_mfma_f32_16x16x32_bf16 v[74:77], v[78:81], v[70:73], v[74:77]
	ds_read_b128 v[78:81], v213 offset:13056
	s_waitcnt lgkmcnt(0)
	v_mfma_f32_16x16x32_bf16 v[78:81], v[78:81], v[50:53], 0
	v_mfma_f32_16x16x32_bf16 v[78:81], v[82:85], v[54:57], v[78:81]
	ds_read_b128 v[82:85], v213 offset:13184
	s_waitcnt lgkmcnt(0)
	v_mfma_f32_16x16x32_bf16 v[78:81], v[82:85], v[58:61], v[78:81]
	ds_read_b128 v[82:85], v213 offset:13248
	ds_read_b128 v[86:89], v213 offset:17472
	s_waitcnt lgkmcnt(1)
	v_mfma_f32_16x16x32_bf16 v[78:81], v[82:85], v[70:73], v[78:81]
	ds_read_b128 v[82:85], v213 offset:17408
	ds_read_b128 v[90:93], v213 offset:21824
	ds_read_b128 v[94:97], v213 offset:26176
	s_waitcnt lgkmcnt(2)
	v_mfma_f32_16x16x32_bf16 v[82:85], v[82:85], v[50:53], 0
	ds_read_b128 v[98:101], v213 offset:30528
	v_mfma_f32_16x16x32_bf16 v[82:85], v[86:89], v[54:57], v[82:85]
	ds_read_b128 v[86:89], v213 offset:17536
	s_waitcnt lgkmcnt(0)
	v_mfma_f32_16x16x32_bf16 v[82:85], v[86:89], v[58:61], v[82:85]
	ds_read_b128 v[86:89], v213 offset:17600
	s_waitcnt lgkmcnt(0)
	v_mfma_f32_16x16x32_bf16 v[82:85], v[86:89], v[70:73], v[82:85]
	ds_read_b128 v[86:89], v213 offset:21760
	s_waitcnt lgkmcnt(0)
	v_mfma_f32_16x16x32_bf16 v[86:89], v[86:89], v[50:53], 0
	v_mfma_f32_16x16x32_bf16 v[86:89], v[90:93], v[54:57], v[86:89]
	ds_read_b128 v[90:93], v213 offset:21888
	s_waitcnt lgkmcnt(0)
	v_mfma_f32_16x16x32_bf16 v[86:89], v[90:93], v[58:61], v[86:89]
	ds_read_b128 v[90:93], v213 offset:21952
	s_waitcnt lgkmcnt(0)
	v_mfma_f32_16x16x32_bf16 v[86:89], v[90:93], v[70:73], v[86:89]
	ds_read_b128 v[90:93], v213 offset:26112
	s_waitcnt lgkmcnt(0)
	v_mfma_f32_16x16x32_bf16 v[90:93], v[90:93], v[50:53], 0
	v_mfma_f32_16x16x32_bf16 v[90:93], v[94:97], v[54:57], v[90:93]
	ds_read_b128 v[94:97], v213 offset:26240
	s_waitcnt lgkmcnt(0)
	v_mfma_f32_16x16x32_bf16 v[90:93], v[94:97], v[58:61], v[90:93]
	ds_read_b128 v[94:97], v213 offset:26304
	s_waitcnt lgkmcnt(0)
	v_mfma_f32_16x16x32_bf16 v[90:93], v[94:97], v[70:73], v[90:93]
	ds_read_b128 v[94:97], v213 offset:30464
	s_waitcnt lgkmcnt(0)
	v_mfma_f32_16x16x32_bf16 v[94:97], v[94:97], v[50:53], 0
	v_mfma_f32_16x16x32_bf16 v[94:97], v[98:101], v[54:57], v[94:97]
	ds_read_b128 v[98:101], v213 offset:30592
	s_waitcnt lgkmcnt(0)
	v_mfma_f32_16x16x32_bf16 v[94:97], v[98:101], v[58:61], v[94:97]
	ds_read_b128 v[98:101], v213 offset:30656
	ds_read_b128 v[102:105], v213 offset:34880
	s_waitcnt lgkmcnt(1)
	v_mfma_f32_16x16x32_bf16 v[94:97], v[98:101], v[70:73], v[94:97]
	ds_read_b128 v[98:101], v213 offset:34816
	ds_read_b128 v[106:109], v213 offset:39232
	ds_read_b128 v[110:113], v213 offset:43584
	s_waitcnt lgkmcnt(2)
	v_mfma_f32_16x16x32_bf16 v[98:101], v[98:101], v[50:53], 0
	ds_read_b128 v[114:117], v213 offset:47936
	v_mfma_f32_16x16x32_bf16 v[98:101], v[102:105], v[54:57], v[98:101]
	ds_read_b128 v[102:105], v213 offset:34944
	s_waitcnt lgkmcnt(0)
	v_mfma_f32_16x16x32_bf16 v[98:101], v[102:105], v[58:61], v[98:101]
	ds_read_b128 v[102:105], v213 offset:35008
	s_waitcnt lgkmcnt(0)
	v_mfma_f32_16x16x32_bf16 v[98:101], v[102:105], v[70:73], v[98:101]
	ds_read_b128 v[102:105], v213 offset:39168
	s_waitcnt lgkmcnt(0)
	v_mfma_f32_16x16x32_bf16 v[102:105], v[102:105], v[50:53], 0
	v_mfma_f32_16x16x32_bf16 v[102:105], v[106:109], v[54:57], v[102:105]
	ds_read_b128 v[106:109], v213 offset:39296
	s_waitcnt lgkmcnt(0)
	v_mfma_f32_16x16x32_bf16 v[102:105], v[106:109], v[58:61], v[102:105]
	ds_read_b128 v[106:109], v213 offset:39360
	s_waitcnt lgkmcnt(0)
	v_mfma_f32_16x16x32_bf16 v[102:105], v[106:109], v[70:73], v[102:105]
	ds_read_b128 v[106:109], v213 offset:43520
	s_waitcnt lgkmcnt(0)
	v_mfma_f32_16x16x32_bf16 v[106:109], v[106:109], v[50:53], 0
	v_mfma_f32_16x16x32_bf16 v[106:109], v[110:113], v[54:57], v[106:109]
	ds_read_b128 v[110:113], v213 offset:43648
	s_waitcnt lgkmcnt(0)
	v_mfma_f32_16x16x32_bf16 v[106:109], v[110:113], v[58:61], v[106:109]
	ds_read_b128 v[110:113], v213 offset:43712
	s_waitcnt lgkmcnt(0)
	v_mfma_f32_16x16x32_bf16 v[106:109], v[110:113], v[70:73], v[106:109]
	ds_read_b128 v[110:113], v213 offset:47872
	s_waitcnt lgkmcnt(0)
	v_mfma_f32_16x16x32_bf16 v[110:113], v[110:113], v[50:53], 0
	v_mfma_f32_16x16x32_bf16 v[110:113], v[114:117], v[54:57], v[110:113]
	ds_read_b128 v[114:117], v213 offset:48000
	s_waitcnt lgkmcnt(0)
	v_mfma_f32_16x16x32_bf16 v[110:113], v[114:117], v[58:61], v[110:113]
	ds_read_b128 v[114:117], v213 offset:48064
	ds_read_b128 v[118:121], v213 offset:52288
	s_waitcnt lgkmcnt(1)
	v_mfma_f32_16x16x32_bf16 v[110:113], v[114:117], v[70:73], v[110:113]
	ds_read_b128 v[114:117], v213 offset:52224
	ds_read_b128 v[122:125], v213 offset:56640
	ds_read_b128 v[126:129], v213 offset:60992
	s_waitcnt lgkmcnt(2)
	v_mfma_f32_16x16x32_bf16 v[114:117], v[114:117], v[50:53], 0
	ds_read_b128 v[132:135], v213 offset:65344
	v_mfma_f32_16x16x32_bf16 v[114:117], v[118:121], v[54:57], v[114:117]
	ds_read_b128 v[118:121], v213 offset:52352
	s_waitcnt lgkmcnt(0)
	v_mfma_f32_16x16x32_bf16 v[114:117], v[118:121], v[58:61], v[114:117]
	ds_read_b128 v[118:121], v213 offset:52416
	s_waitcnt lgkmcnt(0)
	v_mfma_f32_16x16x32_bf16 v[114:117], v[118:121], v[70:73], v[114:117]
	ds_read_b128 v[118:121], v213 offset:56576
	s_waitcnt lgkmcnt(0)
	v_mfma_f32_16x16x32_bf16 v[118:121], v[118:121], v[50:53], 0
	v_mfma_f32_16x16x32_bf16 v[118:121], v[122:125], v[54:57], v[118:121]
	ds_read_b128 v[122:125], v213 offset:56704
	s_waitcnt lgkmcnt(0)
	v_mfma_f32_16x16x32_bf16 v[118:121], v[122:125], v[58:61], v[118:121]
	ds_read_b128 v[122:125], v213 offset:56768
	s_waitcnt lgkmcnt(0)
	v_mfma_f32_16x16x32_bf16 v[118:121], v[122:125], v[70:73], v[118:121]
	ds_read_b128 v[122:125], v213 offset:60928
	s_waitcnt lgkmcnt(0)
	v_mfma_f32_16x16x32_bf16 v[122:125], v[122:125], v[50:53], 0
	v_mfma_f32_16x16x32_bf16 v[122:125], v[126:129], v[54:57], v[122:125]
	ds_read_b128 v[126:129], v213 offset:61056
	s_waitcnt lgkmcnt(0)
	v_mfma_f32_16x16x32_bf16 v[122:125], v[126:129], v[58:61], v[122:125]
	ds_read_b128 v[126:129], v213 offset:61120
	s_waitcnt lgkmcnt(0)
	v_mfma_f32_16x16x32_bf16 v[122:125], v[126:129], v[70:73], v[122:125]
	ds_read_b128 v[126:129], v213 offset:65280
	s_waitcnt lgkmcnt(0)
	v_mfma_f32_16x16x32_bf16 v[126:129], v[126:129], v[50:53], 0
	v_mfma_f32_16x16x32_bf16 v[126:129], v[132:135], v[54:57], v[126:129]
	ds_read_b128 v[132:135], v213 offset:65408
	s_waitcnt lgkmcnt(0)
	v_mfma_f32_16x16x32_bf16 v[126:129], v[132:135], v[58:61], v[126:129]
	ds_read_b128 v[132:135], v213 offset:65472
	s_waitcnt lgkmcnt(0)
	v_mfma_f32_16x16x32_bf16 v[126:129], v[132:135], v[70:73], v[126:129]
	v_mad_u64_u32 v[132:133], s[70:71], v131, s3, v[138:139]
	v_mad_i32_i24 v133, s31, v216, v133
	global_load_dwordx4 v[142:145], v[132:133], off
	global_load_dwordx4 v[146:149], v[132:133], off offset:64
	global_load_dwordx4 v[150:153], v[132:133], off offset:128
	global_load_dwordx4 v[154:157], v[132:133], off offset:192
	v_cndmask_b32_e64 v131, 0, 1, s[94:95]
	v_cmp_ne_u32_e64 s[74:75], 1, v131
	s_mulk_i32 s31, 0x600
	s_cbranch_vccz .LBB0_665
	v_cndmask_b32_e64 v131, 0, 1, s[86:87]
	v_cmp_ne_u32_e64 s[70:71], 1, v131
	s_andn2_b64 vcc, exec, s[86:87]
	s_cbranch_vccz .LBB0_666

	.amdhsa_kernel _Z8yoco_fwd4Args
		.amdhsa_group_segment_fixed_size 0
		.amdhsa_private_segment_fixed_size 0
		.amdhsa_kernarg_size 504
		.amdhsa_user_sgpr_count 2
		.amdhsa_user_sgpr_dispatch_ptr 0
		.amdhsa_user_sgpr_queue_ptr 0
		.amdhsa_user_sgpr_kernarg_segment_ptr 1
		.amdhsa_user_sgpr_dispatch_id 0
		.amdhsa_user_sgpr_kernarg_preload_length 0
		.amdhsa_user_sgpr_kernarg_preload_offset 0
		.amdhsa_user_sgpr_private_segment_size 0
		.amdhsa_uses_dynamic_stack 0
		.amdhsa_enable_private_segment 0
		.amdhsa_system_sgpr_workgroup_id_x 1
		.amdhsa_system_sgpr_workgroup_id_y 0
		.amdhsa_system_sgpr_workgroup_id_z 0
		.amdhsa_system_sgpr_workgroup_info 0
		.amdhsa_system_vgpr_workitem_id 0
		.amdhsa_next_free_vgpr 256
		.amdhsa_next_free_sgpr 102
		.amdhsa_accum_offset 256
		.amdhsa_reserve_vcc 1
		.amdhsa_float_round_mode_32 0
		.amdhsa_float_round_mode_16_64 0
		.amdhsa_float_denorm_mode_32 3
		.amdhsa_float_denorm_mode_16_64 3
		.amdhsa_dx10_clamp 1
		.amdhsa_ieee_mode 1
		.amdhsa_fp16_overflow 0
		.amdhsa_tg_split 0
		.amdhsa_exception_fp_ieee_invalid_op 0
		.amdhsa_exception_fp_denorm_src 0
		.amdhsa_exception_fp_ieee_div_zero 0
		.amdhsa_exception_fp_ieee_overflow 0
		.amdhsa_exception_fp_ieee_underflow 0
		.amdhsa_exception_fp_ieee_inexact 0
		.amdhsa_exception_int_div_zero 0
	.end_amdhsa_kernel

amdhsa.kernels:
  - .agpr_count:     0
    .args:
      - .offset:         0
        .size:           248
        .value_kind:     by_value
      - .offset:         248
        .size:           4
        .value_kind:     hidden_block_count_x
      - .offset:         252
        .size:           4
        .value_kind:     hidden_block_count_y
      - .offset:         256
        .size:           4
        .value_kind:     hidden_block_count_z
      - .offset:         260
        .size:           2
        .value_kind:     hidden_group_size_x
      - .offset:         262
        .size:           2
        .value_kind:     hidden_group_size_y
      - .offset:         264
        .size:           2
        .value_kind:     hidden_group_size_z
      - .offset:         266
        .size:           2
        .value_kind:     hidden_remainder_x
      - .offset:         268
        .size:           2
        .value_kind:     hidden_remainder_y
      - .offset:         270
        .size:           2
        .value_kind:     hidden_remainder_z
      - .offset:         288
        .size:           8
        .value_kind:     hidden_global_offset_x
      - .offset:         296
        .size:           8
        .value_kind:     hidden_global_offset_y
      - .offset:         304
        .size:           8
        .value_kind:     hidden_global_offset_z
      - .offset:         312
        .size:           2
        .value_kind:     hidden_grid_dims
      - .offset:         368
        .size:           4
        .value_kind:     hidden_dynamic_lds_size
    .group_segment_fixed_size: 0
    .kernarg_segment_align: 8
    .kernarg_segment_size: 504
    .language:       OpenCL C
    .language_version:
      - 2
      - 0
    .max_flat_workgroup_size: 512
    .name:           _Z8yoco_fwd4Args
    .private_segment_fixed_size: 0
    .sgpr_count:     108
    .sgpr_spill_count: 38
    .symbol:         _Z8yoco_fwd4Args.kd
    .uniform_work_group_size: 1
    .uses_dynamic_stack: false
    .vgpr_count:     256
    .vgpr_spill_count: 0
    .wavefront_size: 64
